# NA units: per-wave skip of QK^T MFMAs + bias lookups for key tiles whose grid row is outside the wave's 8-row neighbourhood (scores set to -inf directly; bit-identical result)
# speedup vs baseline: 1.0147x; 1.0147x over previous
.LBB0_610:
	s_add_i32 s20, s19, 2
	s_add_i32 s8, s12, s20
	v_cmp_ge_u32_e32 vcc, s8, v169
	v_cmp_lt_u32_e64 s[8:9], s8, v170
	s_nop 1
	s_and_b64 s[8:9], vcc, s[8:9]
	s_cmp_gt_u32 s20, 11
	s_cselect_b64 s[8:9], exec, s[8:9]
	s_cmp_eq_u64 s[8:9], 0
	s_cbranch_scc1 .Lna_deadA
	ds_read_b128 v[64:67], v158 offset:49152
	ds_read_b128 v[240:243], v161 offset:49152
	ds_read_b128 v[244:247], v158 offset:57344
	ds_read_b128 v[248:251], v161 offset:57344
	v_add_f32_e32 v144, 0, v236
	v_add_f32_e32 v144, v238, v144
	v_add_f32_e32 v144, v145, v144
	v_add_f32_e32 v144, v237, v144
	v_add_f32_e32 v144, v146, v144
	v_add_f32_e32 v144, v235, v144
	v_add_f32_e32 v144, v147, v144
	v_add_f32_e32 v144, v234, v144
	v_add_f32_e32 v144, v231, v144
	v_add_f32_e32 v144, v233, v144
	v_add_f32_e32 v144, v230, v144
	v_add_f32_e32 v144, v232, v144
	v_exp_f32_e32 v134, v134
	v_add_f32_e32 v144, v227, v144
	v_exp_f32_e32 v135, v135
	v_add_f32_e32 v144, v229, v144
	v_exp_f32_e32 v138, v138
	v_add_f32_e32 v144, v226, v144
	v_exp_f32_e32 v139, v139
	v_add_f32_e32 v144, v228, v144
	v_exp_f32_e32 v130, v130
	v_add_f32_e32 v144, v134, v144
	v_exp_f32_e32 v131, v131
	v_add_f32_e32 v144, v135, v144
	v_exp_f32_e32 v132, v132
	v_add_f32_e32 v144, v138, v144
	v_exp_f32_e32 v133, v133
	v_add_f32_e32 v144, v139, v144
	v_exp_f32_e32 v136, v136
	v_add_f32_e32 v144, v130, v144
	v_exp_f32_e32 v137, v137
	v_add_f32_e32 v144, v131, v144
	v_exp_f32_e32 v142, v142
	v_add_f32_e32 v144, v132, v144
	v_exp_f32_e32 v143, v143
	v_add_f32_e32 v144, v133, v144
	v_exp_f32_e32 v140, v140
	v_add_f32_e32 v144, v136, v144
	v_exp_f32_e32 v141, v141
	v_add_f32_e32 v144, v137, v144
	v_exp_f32_e32 v128, v128
	v_add_f32_e32 v144, v142, v144
	v_exp_f32_e32 v129, v129
	v_add_f32_e32 v144, v143, v144
	v_add_f32_e32 v144, v140, v144
	v_add_f32_e32 v144, v141, v144
	v_add_f32_e32 v144, v128, v144
	v_add_f32_e32 v223, v129, v144
	v_mov_b32_e32 v224, v223
	v_cvt_pk_bf16_f32 v144, v236, v238
	v_cvt_pk_bf16_f32 v145, v145, v237
	v_cvt_pk_bf16_f32 v146, v146, v235
	s_nop 0
	v_permlane32_swap_b32_e32 v223, v224
	v_cvt_pk_bf16_f32 v147, v147, v234
	v_permlane32_swap_b32_e32 v144, v146
	v_cvt_pk_bf16_f32 v234, v231, v233
	v_cvt_pk_bf16_f32 v235, v230, v232
	v_cvt_pk_bf16_f32 v236, v227, v229
	v_cvt_pk_bf16_f32 v237, v226, v228
	v_cvt_pk_bf16_f32 v226, v134, v135
	v_cvt_pk_bf16_f32 v227, v138, v139
	v_cvt_pk_bf16_f32 v228, v130, v131
	v_cvt_pk_bf16_f32 v229, v132, v133
	v_cvt_pk_bf16_f32 v230, v136, v137
	v_cvt_pk_bf16_f32 v231, v142, v143
	v_cvt_pk_bf16_f32 v232, v140, v141
	v_cvt_pk_bf16_f32 v233, v128, v129
	v_permlane32_swap_b32_e32 v145, v147
	v_permlane32_swap_b32_e32 v234, v236
	v_permlane32_swap_b32_e32 v235, v237
	v_permlane32_swap_b32_e32 v226, v228
	v_permlane32_swap_b32_e32 v227, v229
	v_permlane32_swap_b32_e32 v230, v232
	v_permlane32_swap_b32_e32 v231, v233
	s_add_i32 s8, s19, 3
	s_cmp_lt_u32 s8, 12
	s_cselect_b64 s[10:11], -1, 0
	s_and_b64 s[8:9], s[10:11], exec
	s_cselect_b32 s8, 0, -12
	s_cselect_b32 s9, s13, 0x4000
	s_add_i32 s8, s8, s19
	s_lshl_b32 s8, s8, 6
	s_add_i32 s8, s8, s9
	s_mulk_i32 s8, 0x2400
	s_add_i32 s21, s8, 0x1b0000
	s_add_u32 s8, s14, s21
	s_addc_u32 s9, s15, 0
	s_add_u32 vcc_lo, s16, s21
	s_addc_u32 vcc_hi, s17, 0
	v_lshl_add_u64 v[128:129], vcc, 0, v[192:193]
	v_lshl_add_u64 v[132:133], vcc, 0, v[150:151]
	v_lshl_add_u64 v[136:137], s[8:9], 0, v[192:193]
	v_lshl_add_u64 v[140:141], s[8:9], 0, v[150:151]
	global_load_dwordx4 v[128:131], v[128:129], off
	s_nop 0
	global_load_dwordx4 v[132:135], v[132:133], off
	s_nop 0
	global_load_dwordx4 v[136:139], v[136:137], off
	s_nop 0
	global_load_dwordx4 v[140:143], v[140:141], off
	s_cmp_gt_u32 s20, 11
	s_waitcnt lgkmcnt(3)
	v_mfma_f32_32x32x16_bf16 v[80:95], v[64:67], v[100:103], 0
	s_waitcnt lgkmcnt(2)
	v_mfma_f32_32x32x16_bf16 v[80:95], v[240:243], v[104:107], v[80:95]
	ds_read_b128 v[240:243], v162 offset:49152
	s_waitcnt lgkmcnt(2)
	v_mfma_f32_32x32x16_bf16 v[64:79], v[244:247], v[100:103], 0
	ds_read_b128 v[244:247], v162 offset:57344
	s_waitcnt lgkmcnt(2)
	v_mfma_f32_32x32x16_bf16 v[64:79], v[248:251], v[104:107], v[64:79]
	ds_read_b128 v[248:251], v160 offset:49152
	s_waitcnt lgkmcnt(2)
	v_mfma_f32_32x32x16_bf16 v[80:95], v[240:243], v[120:123], v[80:95]
	ds_read_b128 v[240:243], v160 offset:57344
	s_waitcnt lgkmcnt(2)
	v_mfma_f32_32x32x16_bf16 v[64:79], v[244:247], v[120:123], v[64:79]
	ds_read_b128 v[244:247], v166 offset:49152
	s_waitcnt lgkmcnt(2)
	v_mfma_f32_32x32x16_bf16 v[80:95], v[248:251], v[124:127], v[80:95]
	ds_read_b128 v[248:251], v166 offset:57344
	s_waitcnt lgkmcnt(2)
	v_mfma_f32_32x32x16_bf16 v[64:79], v[240:243], v[124:127], v[64:79]
	ds_read_b128 v[240:243], v165 offset:49152
	s_waitcnt lgkmcnt(2)
	v_mfma_f32_32x32x16_bf16 v[80:95], v[244:247], v[116:119], v[80:95]
	ds_read_b128 v[244:247], v165 offset:57344
	s_waitcnt lgkmcnt(2)
	v_mfma_f32_32x32x16_bf16 v[64:79], v[248:251], v[116:119], v[64:79]
	ds_read_b128 v[248:251], v164 offset:49152
	s_waitcnt lgkmcnt(2)
	v_mfma_f32_32x32x16_bf16 v[80:95], v[240:243], v[112:115], v[80:95]
	ds_read_b128 v[240:243], v164 offset:57344
	s_waitcnt lgkmcnt(2)
	v_mfma_f32_32x32x16_bf16 v[64:79], v[244:247], v[112:115], v[64:79]
	ds_read_b128 v[244:247], v163 offset:49152
	s_waitcnt lgkmcnt(2)
	v_mfma_f32_32x32x16_bf16 v[80:95], v[248:251], v[108:111], v[80:95]
	ds_read_b128 v[248:251], v163 offset:57344
	s_waitcnt lgkmcnt(2)
	v_mfma_f32_32x32x16_bf16 v[64:79], v[240:243], v[108:111], v[64:79]
	s_waitcnt lgkmcnt(1)
	v_mfma_f32_32x32x16_bf16 v[80:95], v[244:247], v[96:99], v[80:95]
	s_waitcnt lgkmcnt(0)
	v_mfma_f32_32x32x16_bf16 v[64:79], v[248:251], v[96:99], v[64:79]
	s_cbranch_scc1 .LBB0_612
	v_add3_u32 v219, v215, s19, 2
	v_max_i32_e32 v219, -7, v219
	v_add_u32_e32 v219, 7, v219
	s_add_i32 s8, s12, s19
	v_min_u32_e32 v219, 14, v219
	s_add_i32 s8, s8, 2
	v_mul_u32_u24_e32 v219, 31, v219
	v_cmp_ge_u32_e32 vcc, s8, v169
	v_cmp_lt_u32_e64 s[8:9], s8, v170
	v_sub_u32_e32 v219, v219, v168
	s_and_b64 s[8:9], vcc, s[8:9]
	v_add_u32_e32 v219, 15, v219
	v_mov_b32_e32 v218, 0x1d1
	v_add_u32_e32 v239, v219, v173
	s_and_b64 vcc, s[36:37], s[8:9]
	v_cndmask_b32_e32 v239, v218, v239, vcc
	v_lshl_add_u32 v239, v239, 2, s18
	ds_read_b32 v239, v239
	v_readlane_b32 s10, v255, 28
	v_readlane_b32 s11, v255, 29
	v_readlane_b32 s22, v255, 30
	s_and_b64 s[10:11], s[8:9], s[10:11]
	v_add_u32_e32 v240, v219, v174
	s_and_b64 vcc, s[38:39], s[8:9]
	v_cndmask_b32_e32 v240, v218, v240, vcc
	v_lshl_add_u32 v240, v240, 2, s18
	ds_read_b32 v240, v240
	v_readlane_b32 s23, v255, 31
	v_add_u32_e32 v241, v219, v175
	s_and_b64 vcc, s[40:41], s[8:9]
	v_cndmask_b32_e32 v241, v218, v241, vcc
	v_lshl_add_u32 v241, v241, 2, s18
	ds_read_b32 v241, v241
	v_add_u32_e32 v242, v219, v176
	s_and_b64 vcc, s[42:43], s[8:9]
	v_cndmask_b32_e32 v242, v218, v242, vcc
	v_lshl_add_u32 v242, v242, 2, s18
	ds_read_b32 v242, v242
	v_add_u32_e32 v243, v219, v177
	s_and_b64 vcc, s[8:9], s[44:45]
	v_cndmask_b32_e32 v243, v218, v243, vcc
	v_lshl_add_u32 v243, v243, 2, s18
	ds_read_b32 v243, v243
	v_add_u32_e32 v244, v219, v178
	s_and_b64 vcc, s[8:9], s[46:47]
	v_cndmask_b32_e32 v244, v218, v244, vcc
	v_lshl_add_u32 v244, v244, 2, s18
	ds_read_b32 v244, v244
	v_add_u32_e32 v245, v219, v179
	s_and_b64 vcc, s[8:9], s[48:49]
	v_cndmask_b32_e32 v245, v218, v245, vcc
	v_lshl_add_u32 v245, v245, 2, s18
	ds_read_b32 v245, v245
	v_add_u32_e32 v246, v219, v180
	s_and_b64 vcc, s[8:9], s[50:51]
	v_cndmask_b32_e32 v246, v218, v246, vcc
	v_lshl_add_u32 v246, v246, 2, s18
	ds_read_b32 v246, v246
	v_add_u32_e32 v247, v219, v181
	s_and_b64 vcc, s[10:11], s[22:23]
	v_cndmask_b32_e32 v247, v218, v247, vcc
	v_lshl_add_u32 v247, v247, 2, s18
	ds_read_b32 v247, v247
	v_readlane_b32 s10, v255, 32
	v_readlane_b32 s11, v255, 33
	v_readlane_b32 s22, v255, 34
	s_and_b64 s[10:11], s[8:9], s[10:11]
	v_readlane_b32 s23, v255, 35
	v_add_u32_e32 v248, v219, v182
	s_and_b64 vcc, s[10:11], s[22:23]
	v_cndmask_b32_e32 v248, v218, v248, vcc
	v_lshl_add_u32 v248, v248, 2, s18
	ds_read_b32 v248, v248
	v_readlane_b32 s10, v255, 36
	v_readlane_b32 s11, v255, 37
	v_readlane_b32 s22, v255, 38
	s_and_b64 s[10:11], s[8:9], s[10:11]
	v_readlane_b32 s23, v255, 39
	v_add_u32_e32 v249, v219, v183
	s_and_b64 vcc, s[10:11], s[22:23]
	v_cndmask_b32_e32 v249, v218, v249, vcc
	v_lshl_add_u32 v249, v249, 2, s18
	ds_read_b32 v249, v249
	v_readlane_b32 s10, v255, 40
	v_readlane_b32 s11, v255, 41
	v_readlane_b32 s22, v255, 42
	s_and_b64 s[10:11], s[8:9], s[10:11]
	v_readlane_b32 s23, v255, 43
	v_add_u32_e32 v250, v219, v184
	s_and_b64 vcc, s[10:11], s[22:23]
	v_cndmask_b32_e32 v250, v218, v250, vcc
	v_lshl_add_u32 v250, v250, 2, s18
	ds_read_b32 v250, v250
	v_readlane_b32 s10, v255, 44
	v_readlane_b32 s11, v255, 45
	s_and_b64 s[10:11], s[8:9], s[10:11]
	v_add_u32_e32 v251, v219, v185
	s_and_b64 vcc, s[10:11], s[30:31]
	v_cndmask_b32_e32 v251, v218, v251, vcc
	v_lshl_add_u32 v251, v251, 2, s18
	ds_read_b32 v251, v251
	s_and_b64 s[10:11], s[8:9], s[34:35]
	v_add_u32_e32 v252, v219, v186
	s_and_b64 vcc, s[10:11], s[24:25]
	v_cndmask_b32_e32 v252, v218, v252, vcc
	v_lshl_add_u32 v252, v252, 2, s18
	ds_read_b32 v252, v252
	s_and_b64 s[10:11], s[8:9], s[26:27]
	v_add_u32_e32 v253, v219, v187
	s_and_b64 vcc, s[10:11], s[28:29]
	v_cndmask_b32_e32 v253, v218, v253, vcc
	v_lshl_add_u32 v253, v253, 2, s18
	ds_read_b32 v253, v253
	s_and_b64 s[10:11], s[8:9], s[52:53]
	s_waitcnt lgkmcnt(14)
	v_add_f32_e32 v80, v80, v239
	v_add_u32_e32 v239, v219, v188
	s_and_b64 vcc, s[10:11], s[54:55]
	v_cndmask_b32_e32 v239, v218, v239, vcc
	v_lshl_add_u32 v239, v239, 2, s18
	ds_read_b32 v239, v239
	s_and_b64 s[10:11], s[8:9], s[56:57]
	s_waitcnt lgkmcnt(14)
	v_add_f32_e32 v81, v81, v240
	v_add_u32_e32 v240, v219, v189
	s_and_b64 vcc, s[10:11], s[58:59]
	v_cndmask_b32_e32 v240, v218, v240, vcc
	v_lshl_add_u32 v240, v240, 2, s18
	ds_read_b32 v240, v240
	s_and_b64 s[10:11], s[8:9], s[60:61]
	s_waitcnt lgkmcnt(14)
	v_add_f32_e32 v82, v82, v241
	v_add_u32_e32 v241, v219, v190
	s_and_b64 vcc, s[10:11], s[62:63]
	v_cndmask_b32_e32 v241, v218, v241, vcc
	v_lshl_add_u32 v241, v241, 2, s18
	ds_read_b32 v241, v241
	s_and_b64 s[10:11], s[8:9], s[64:65]
	s_waitcnt lgkmcnt(14)
	v_add_f32_e32 v83, v83, v242
	v_add_u32_e32 v242, v219, v191
	s_and_b64 vcc, s[10:11], s[66:67]
	v_cndmask_b32_e32 v242, v218, v242, vcc
	v_lshl_add_u32 v242, v242, 2, s18
	ds_read_b32 v242, v242
	s_and_b64 s[10:11], s[8:9], s[68:69]
	s_waitcnt lgkmcnt(14)
	v_add_f32_e32 v84, v84, v243
	v_add_u32_e32 v243, v219, v200
	s_and_b64 vcc, s[10:11], s[70:71]
	v_cndmask_b32_e32 v243, v218, v243, vcc
	v_lshl_add_u32 v243, v243, 2, s18
	ds_read_b32 v243, v243
	s_and_b64 s[10:11], s[8:9], s[72:73]
	s_waitcnt lgkmcnt(14)
	v_add_f32_e32 v85, v85, v244
	v_add_u32_e32 v244, v219, v201
	s_and_b64 vcc, s[10:11], s[74:75]
	v_cndmask_b32_e32 v244, v218, v244, vcc
	v_lshl_add_u32 v244, v244, 2, s18
	ds_read_b32 v244, v244
	s_and_b64 s[10:11], s[8:9], s[76:77]
	s_waitcnt lgkmcnt(14)
	v_add_f32_e32 v86, v86, v245
	v_add_u32_e32 v245, v219, v203
	s_and_b64 vcc, s[10:11], s[78:79]
	v_cndmask_b32_e32 v245, v218, v245, vcc
	v_lshl_add_u32 v245, v245, 2, s18
	ds_read_b32 v245, v245
	s_and_b64 s[10:11], s[8:9], s[80:81]
	s_waitcnt lgkmcnt(14)
	v_add_f32_e32 v87, v87, v246
	v_add_u32_e32 v246, v219, v204
	s_and_b64 vcc, s[10:11], s[82:83]
	v_cndmask_b32_e32 v246, v218, v246, vcc
	v_lshl_add_u32 v246, v246, 2, s18
	ds_read_b32 v246, v246
	s_and_b64 s[10:11], s[8:9], s[84:85]
	s_waitcnt lgkmcnt(14)
	v_add_f32_e32 v88, v88, v247
	v_add_u32_e32 v247, v219, v205
	s_and_b64 vcc, s[10:11], s[86:87]
	v_cndmask_b32_e32 v247, v218, v247, vcc
	v_lshl_add_u32 v247, v247, 2, s18
	ds_read_b32 v247, v247
	s_waitcnt lgkmcnt(14)
	v_add_f32_e32 v89, v89, v248
	v_add_u32_e32 v248, v219, v206
	s_and_b64 vcc, s[8:9], s[88:89]
	v_cndmask_b32_e32 v248, v218, v248, vcc
	v_lshl_add_u32 v248, v248, 2, s18
	ds_read_b32 v248, v248
	s_waitcnt lgkmcnt(14)
	v_add_f32_e32 v90, v90, v249
	v_add_u32_e32 v249, v219, v207
	s_and_b64 vcc, s[8:9], s[90:91]
	v_cndmask_b32_e32 v249, v218, v249, vcc
	v_lshl_add_u32 v249, v249, 2, s18
	ds_read_b32 v249, v249
	s_waitcnt lgkmcnt(14)
	v_add_f32_e32 v91, v91, v250
	v_add_u32_e32 v250, v219, v208
	s_and_b64 vcc, s[8:9], s[92:93]
	v_cndmask_b32_e32 v250, v218, v250, vcc
	v_lshl_add_u32 v250, v250, 2, s18
	ds_read_b32 v250, v250
	s_waitcnt lgkmcnt(14)
	v_add_f32_e32 v92, v92, v251
	v_add_u32_e32 v251, v219, v209
	s_and_b64 vcc, s[8:9], s[94:95]
	v_cndmask_b32_e32 v251, v218, v251, vcc
	v_lshl_add_u32 v251, v251, 2, s18
	ds_read_b32 v251, v251
	s_waitcnt lgkmcnt(14)
	v_add_f32_e32 v93, v93, v252
	v_add_u32_e32 v252, v219, v210
	s_and_b64 vcc, s[8:9], s[96:97]
	v_cndmask_b32_e32 v252, v218, v252, vcc
	v_lshl_add_u32 v252, v252, 2, s18
	ds_read_b32 v252, v252
	s_waitcnt lgkmcnt(14)
	v_add_f32_e32 v94, v94, v253
	v_add_u32_e32 v253, v219, v211
	s_and_b64 vcc, s[8:9], s[2:3]
	v_cndmask_b32_e32 v253, v218, v253, vcc
	v_lshl_add_u32 v253, v253, 2, s18
	ds_read_b32 v253, v253
	s_waitcnt lgkmcnt(14)
	v_add_f32_e32 v95, v95, v239
	v_add_u32_e32 v239, v219, v212
	s_and_b64 vcc, s[8:9], s[0:1]
	v_cndmask_b32_e32 v239, v218, v239, vcc
	v_lshl_add_u32 v239, v239, 2, s18
	ds_read_b32 v239, v239
	s_waitcnt lgkmcnt(14)
	v_add_f32_e32 v64, v64, v240
	v_add_u32_e32 v240, v219, v213
	s_and_b64 vcc, s[8:9], s[6:7]
	v_cndmask_b32_e32 v240, v218, v240, vcc
	v_lshl_add_u32 v240, v240, 2, s18
	ds_read_b32 v240, v240
	s_waitcnt lgkmcnt(14)
	v_add_f32_e32 v65, v65, v241
	s_waitcnt lgkmcnt(13)
	v_add_f32_e32 v66, v66, v242
	s_waitcnt lgkmcnt(12)
	v_add_f32_e32 v67, v67, v243
	s_waitcnt lgkmcnt(11)
	v_add_f32_e32 v68, v68, v244
	s_waitcnt lgkmcnt(10)
	v_add_f32_e32 v69, v69, v245
	s_waitcnt lgkmcnt(9)
	v_add_f32_e32 v70, v70, v246
	s_waitcnt lgkmcnt(8)
	v_add_f32_e32 v71, v71, v247
	s_waitcnt lgkmcnt(7)
	v_add_f32_e32 v72, v72, v248
	s_waitcnt lgkmcnt(6)
	v_add_f32_e32 v73, v73, v249
	s_waitcnt lgkmcnt(5)
	v_add_f32_e32 v74, v74, v250
	s_waitcnt lgkmcnt(4)
	v_add_f32_e32 v75, v75, v251
	s_waitcnt lgkmcnt(3)
	v_add_f32_e32 v76, v76, v252
	s_waitcnt lgkmcnt(2)
	v_add_f32_e32 v77, v77, v253
	s_waitcnt lgkmcnt(1)
	v_add_f32_e32 v78, v78, v239
	s_waitcnt lgkmcnt(0)
	v_add_f32_e32 v79, v79, v240

.LBB0_616:
	v_cndmask_b32_e64 v222, v144, v222, s[8:9]
	v_mul_f32_e32 v144, 0xbe0293ee, v222
	v_fmamk_f32 v80, v80, 0x3e0293ee, v144
	v_fmamk_f32 v81, v81, 0x3e0293ee, v144
	v_fmamk_f32 v82, v82, 0x3e0293ee, v144
	v_fmamk_f32 v83, v83, 0x3e0293ee, v144
	v_fmamk_f32 v84, v84, 0x3e0293ee, v144
	v_fmamk_f32 v85, v85, 0x3e0293ee, v144
	v_fmamk_f32 v86, v86, 0x3e0293ee, v144
	v_fmamk_f32 v87, v87, 0x3e0293ee, v144
	v_fmamk_f32 v88, v88, 0x3e0293ee, v144
	v_fmamk_f32 v89, v89, 0x3e0293ee, v144
	v_fmamk_f32 v90, v90, 0x3e0293ee, v144
	v_fmamk_f32 v91, v91, 0x3e0293ee, v144
	v_fmamk_f32 v92, v92, 0x3e0293ee, v144
	v_fmamk_f32 v93, v93, 0x3e0293ee, v144
	v_fmamk_f32 v94, v94, 0x3e0293ee, v144
	v_fmamk_f32 v95, v95, 0x3e0293ee, v144
	v_exp_f32_e32 v141, v80
	v_exp_f32_e32 v143, v81
	v_exp_f32_e32 v139, v82
	v_exp_f32_e32 v142, v83
	v_exp_f32_e32 v137, v84
	v_exp_f32_e32 v140, v85
	v_exp_f32_e32 v136, v86
	v_exp_f32_e32 v138, v87
	v_exp_f32_e32 v133, v88
	v_exp_f32_e32 v135, v89
	v_exp_f32_e32 v131, v90
	v_exp_f32_e32 v134, v91
	v_exp_f32_e32 v129, v92
	v_exp_f32_e32 v132, v93
	v_exp_f32_e32 v128, v94
	v_exp_f32_e32 v130, v95
	v_fmamk_f32 v145, v64, 0x3e0293ee, v144
	v_fmamk_f32 v146, v65, 0x3e0293ee, v144
	v_fmamk_f32 v147, v66, 0x3e0293ee, v144
	v_fmamk_f32 v226, v67, 0x3e0293ee, v144
	v_fmamk_f32 v227, v68, 0x3e0293ee, v144
	v_fmamk_f32 v228, v69, 0x3e0293ee, v144
	v_fmamk_f32 v229, v70, 0x3e0293ee, v144
	v_fmamk_f32 v230, v71, 0x3e0293ee, v144
	v_fmamk_f32 v231, v72, 0x3e0293ee, v144
	v_fmamk_f32 v232, v73, 0x3e0293ee, v144
	v_fmamk_f32 v233, v74, 0x3e0293ee, v144
	v_fmamk_f32 v234, v75, 0x3e0293ee, v144
	v_fmamk_f32 v235, v76, 0x3e0293ee, v144
	v_fmamk_f32 v236, v77, 0x3e0293ee, v144
	v_fmamk_f32 v237, v78, 0x3e0293ee, v144
	v_fmac_f32_e32 v144, 0x3e0293ee, v79
	s_waitcnt lgkmcnt(0)
	s_barrier
	s_add_i32 s8, s12, s19
	s_add_i32 s8, s8, 3
	v_cmp_ge_u32_e32 vcc, s8, v169
	v_cmp_lt_u32_e64 s[8:9], s8, v170
	s_nop 1
	s_and_b64 s[8:9], vcc, s[8:9]
	s_andn2_b64 s[22:23], exec, s[10:11]
	s_or_b64 s[8:9], s[8:9], s[22:23]
	s_cmp_eq_u64 s[8:9], 0
	s_cbranch_scc1 .Lna_deadB
	ds_read_b128 v[64:67], v158 offset:32768
	ds_read_b128 v[250:253], v161 offset:32768
	s_andn2_b64 vcc, exec, s[10:11]
	v_exp_f32_e32 v249, v144
	v_add_f32_e32 v144, 0, v141
	v_add_f32_e32 v144, v143, v144
	v_add_f32_e32 v144, v139, v144
	v_add_f32_e32 v144, v142, v144
	v_add_f32_e32 v144, v137, v144
	v_add_f32_e32 v144, v140, v144
	v_add_f32_e32 v144, v136, v144
	v_add_f32_e32 v144, v138, v144
	v_add_f32_e32 v144, v133, v144
	v_add_f32_e32 v144, v135, v144
	v_add_f32_e32 v144, v131, v144
	v_add_f32_e32 v144, v134, v144
	v_exp_f32_e32 v218, v145
	v_add_f32_e32 v144, v129, v144
	v_exp_f32_e32 v219, v146
	v_add_f32_e32 v144, v132, v144
	v_exp_f32_e32 v220, v147
	v_add_f32_e32 v144, v128, v144
	v_exp_f32_e32 v221, v226
	v_add_f32_e32 v144, v130, v144
	v_exp_f32_e32 v238, v227
	v_add_f32_e32 v144, v218, v144
	v_exp_f32_e32 v241, v228
	v_add_f32_e32 v144, v219, v144
	v_exp_f32_e32 v242, v229
	v_add_f32_e32 v144, v220, v144
	v_exp_f32_e32 v243, v230
	v_add_f32_e32 v144, v221, v144
	v_exp_f32_e32 v244, v231
	v_add_f32_e32 v144, v238, v144
	v_exp_f32_e32 v245, v232
	v_add_f32_e32 v144, v241, v144
	v_exp_f32_e32 v246, v233
	v_add_f32_e32 v144, v242, v144
	v_exp_f32_e32 v247, v234
	v_add_f32_e32 v144, v243, v144
	v_exp_f32_e32 v248, v235
	v_add_f32_e32 v144, v244, v144
	v_exp_f32_e32 v236, v236
	v_add_f32_e32 v144, v245, v144
	v_exp_f32_e32 v237, v237
	v_add_f32_e32 v144, v246, v144
	v_add_f32_e32 v144, v247, v144
	v_add_f32_e32 v144, v248, v144
	v_add_f32_e32 v144, v236, v144
	v_add_f32_e32 v144, v237, v144
	v_add_f32_e32 v239, v249, v144
	v_mov_b32_e32 v240, v239
	v_cvt_pk_bf16_f32 v144, v141, v143
	v_cvt_pk_bf16_f32 v145, v139, v142
	v_cvt_pk_bf16_f32 v146, v137, v140
	v_cvt_pk_bf16_f32 v147, v136, v138
	s_nop 1
	v_permlane32_swap_b32_e32 v239, v240
	v_permlane32_swap_b32_e32 v144, v146
	v_permlane32_swap_b32_e32 v145, v147
	v_cvt_pk_bf16_f32 v226, v133, v135
	v_cvt_pk_bf16_f32 v227, v131, v134
	v_cvt_pk_bf16_f32 v228, v129, v132
	v_cvt_pk_bf16_f32 v229, v128, v130
	v_cvt_pk_bf16_f32 v230, v218, v219
	v_cvt_pk_bf16_f32 v231, v220, v221
	v_cvt_pk_bf16_f32 v232, v238, v241
	v_cvt_pk_bf16_f32 v233, v242, v243
	v_cvt_pk_bf16_f32 v234, v244, v245
	v_cvt_pk_bf16_f32 v235, v246, v247
	v_cvt_pk_bf16_f32 v236, v248, v236
	v_cvt_pk_bf16_f32 v237, v237, v249
	s_nop 0
	v_permlane32_swap_b32_e32 v226, v228
	v_permlane32_swap_b32_e32 v227, v229
	v_permlane32_swap_b32_e32 v230, v232
	v_permlane32_swap_b32_e32 v231, v233
	v_permlane32_swap_b32_e32 v234, v236
	v_permlane32_swap_b32_e32 v235, v237
	ds_read_b128 v[242:245], v158 offset:40960
	ds_read_b128 v[246:249], v161 offset:40960
	s_cmp_lt_u32 s20, 10
	s_cselect_b32 s8, 0, -12
	s_cselect_b32 s9, s13, 0x4000
	s_add_i32 s8, s8, s19
	s_lshl_b32 s8, s8, 6
	s_add_i32 s8, s8, s9
	s_mulk_i32 s8, 0x2400
	s_add_i32 s10, s8, 0x240000
	s_add_u32 s8, s14, s10
	s_addc_u32 s9, s15, 0
	s_add_u32 s10, s16, s10
	s_addc_u32 s11, s17, 0
	v_lshl_add_u64 v[128:129], s[10:11], 0, v[192:193]
	v_lshl_add_u64 v[132:133], s[10:11], 0, v[150:151]
	v_lshl_add_u64 v[136:137], s[8:9], 0, v[192:193]
	v_lshl_add_u64 v[140:141], s[8:9], 0, v[150:151]
	global_load_dwordx4 v[128:131], v[128:129], off
	s_nop 0
	global_load_dwordx4 v[132:135], v[132:133], off
	s_nop 0
	global_load_dwordx4 v[136:139], v[136:137], off
	s_nop 0
	global_load_dwordx4 v[140:143], v[140:141], off
	s_waitcnt lgkmcnt(3)
	v_mfma_f32_32x32x16_bf16 v[80:95], v[64:67], v[100:103], 0
	s_waitcnt lgkmcnt(2)
	v_mfma_f32_32x32x16_bf16 v[80:95], v[250:253], v[104:107], v[80:95]
	ds_read_b128 v[250:253], v162 offset:32768
	s_waitcnt lgkmcnt(2)
	v_mfma_f32_32x32x16_bf16 v[64:79], v[242:245], v[100:103], 0
	ds_read_b128 v[242:245], v162 offset:40960
	s_waitcnt lgkmcnt(2)
	v_mfma_f32_32x32x16_bf16 v[64:79], v[246:249], v[104:107], v[64:79]
	ds_read_b128 v[246:249], v160 offset:32768
	s_waitcnt lgkmcnt(2)
	v_mfma_f32_32x32x16_bf16 v[80:95], v[250:253], v[120:123], v[80:95]
	ds_read_b128 v[250:253], v160 offset:40960
	s_waitcnt lgkmcnt(2)
	v_mfma_f32_32x32x16_bf16 v[64:79], v[242:245], v[120:123], v[64:79]
	ds_read_b128 v[242:245], v166 offset:32768
	s_waitcnt lgkmcnt(2)
	v_mfma_f32_32x32x16_bf16 v[80:95], v[246:249], v[124:127], v[80:95]
	ds_read_b128 v[246:249], v166 offset:40960
	s_waitcnt lgkmcnt(2)
	v_mfma_f32_32x32x16_bf16 v[64:79], v[250:253], v[124:127], v[64:79]
	ds_read_b128 v[250:253], v165 offset:32768
	s_waitcnt lgkmcnt(2)
	v_mfma_f32_32x32x16_bf16 v[80:95], v[242:245], v[116:119], v[80:95]
	ds_read_b128 v[242:245], v165 offset:40960
	s_waitcnt lgkmcnt(2)
	v_mfma_f32_32x32x16_bf16 v[64:79], v[246:249], v[116:119], v[64:79]
	ds_read_b128 v[246:249], v164 offset:32768
	s_waitcnt lgkmcnt(2)
	v_mfma_f32_32x32x16_bf16 v[80:95], v[250:253], v[112:115], v[80:95]
	ds_read_b128 v[250:253], v164 offset:40960
	s_waitcnt lgkmcnt(2)
	v_mfma_f32_32x32x16_bf16 v[64:79], v[242:245], v[112:115], v[64:79]
	ds_read_b128 v[242:245], v163 offset:32768
	s_waitcnt lgkmcnt(2)
	v_mfma_f32_32x32x16_bf16 v[80:95], v[246:249], v[108:111], v[80:95]
	ds_read_b128 v[246:249], v163 offset:40960
	s_waitcnt lgkmcnt(2)
	v_mfma_f32_32x32x16_bf16 v[64:79], v[250:253], v[108:111], v[64:79]
	s_waitcnt lgkmcnt(1)
	v_mfma_f32_32x32x16_bf16 v[80:95], v[242:245], v[96:99], v[80:95]
	s_waitcnt lgkmcnt(0)
	v_mfma_f32_32x32x16_bf16 v[64:79], v[246:249], v[96:99], v[64:79]
	s_cbranch_vccnz .LBB0_618
	v_add3_u32 v218, v215, s19, 3
	v_max_i32_e32 v218, -7, v218
	v_add_u32_e32 v218, 7, v218
	s_add_i32 s8, s12, s19
	v_min_u32_e32 v218, 14, v218
	s_add_i32 s8, s8, 3
	v_mul_u32_u24_e32 v218, 31, v218
	v_cmp_ge_u32_e32 vcc, s8, v169
	v_cmp_lt_u32_e64 s[8:9], s8, v170
	v_sub_u32_e32 v218, v218, v168
	s_and_b64 s[8:9], vcc, s[8:9]
	v_add_u32_e32 v219, 15, v218
	v_mov_b32_e32 v218, 0x1d1
	v_add_u32_e32 v220, v219, v173
	s_and_b64 vcc, s[36:37], s[8:9]
	v_cndmask_b32_e32 v220, v218, v220, vcc
	v_lshl_add_u32 v220, v220, 2, s18
	ds_read_b32 v220, v220
	v_readlane_b32 s10, v255, 28
	v_readlane_b32 s11, v255, 29
	v_readlane_b32 s22, v255, 30
	s_and_b64 s[10:11], s[8:9], s[10:11]
	v_add_u32_e32 v221, v219, v174
	s_and_b64 vcc, s[38:39], s[8:9]
	v_cndmask_b32_e32 v221, v218, v221, vcc
	v_lshl_add_u32 v221, v221, 2, s18
	ds_read_b32 v221, v221
	v_readlane_b32 s23, v255, 31
	v_add_u32_e32 v241, v219, v175
	s_and_b64 vcc, s[40:41], s[8:9]
	v_cndmask_b32_e32 v241, v218, v241, vcc
	v_lshl_add_u32 v241, v241, 2, s18
	ds_read_b32 v241, v241
	v_add_u32_e32 v242, v219, v176
	s_and_b64 vcc, s[42:43], s[8:9]
	v_cndmask_b32_e32 v242, v218, v242, vcc
	v_lshl_add_u32 v242, v242, 2, s18
	ds_read_b32 v242, v242
	v_add_u32_e32 v243, v219, v177
	s_and_b64 vcc, s[8:9], s[44:45]
	v_cndmask_b32_e32 v243, v218, v243, vcc
	v_lshl_add_u32 v243, v243, 2, s18
	ds_read_b32 v243, v243
	v_add_u32_e32 v244, v219, v178
	s_and_b64 vcc, s[8:9], s[46:47]
	v_cndmask_b32_e32 v244, v218, v244, vcc
	v_lshl_add_u32 v244, v244, 2, s18
	ds_read_b32 v244, v244
	v_add_u32_e32 v245, v219, v179
	s_and_b64 vcc, s[8:9], s[48:49]
	v_cndmask_b32_e32 v245, v218, v245, vcc
	v_lshl_add_u32 v245, v245, 2, s18
	ds_read_b32 v245, v245
	v_add_u32_e32 v246, v219, v180
	s_and_b64 vcc, s[8:9], s[50:51]
	v_cndmask_b32_e32 v246, v218, v246, vcc
	v_lshl_add_u32 v246, v246, 2, s18
	ds_read_b32 v246, v246
	v_add_u32_e32 v247, v219, v181
	s_and_b64 vcc, s[10:11], s[22:23]
	v_cndmask_b32_e32 v247, v218, v247, vcc
	v_lshl_add_u32 v247, v247, 2, s18
	ds_read_b32 v247, v247
	v_readlane_b32 s10, v255, 32
	v_readlane_b32 s11, v255, 33
	v_readlane_b32 s22, v255, 34
	s_and_b64 s[10:11], s[8:9], s[10:11]
	v_readlane_b32 s23, v255, 35
	v_add_u32_e32 v248, v219, v182
	s_and_b64 vcc, s[10:11], s[22:23]
	v_cndmask_b32_e32 v248, v218, v248, vcc
	v_lshl_add_u32 v248, v248, 2, s18
	ds_read_b32 v248, v248
	v_readlane_b32 s10, v255, 36
	v_readlane_b32 s11, v255, 37
	v_readlane_b32 s22, v255, 38
	s_and_b64 s[10:11], s[8:9], s[10:11]
	v_readlane_b32 s23, v255, 39
	v_add_u32_e32 v249, v219, v183
	s_and_b64 vcc, s[10:11], s[22:23]
	v_cndmask_b32_e32 v249, v218, v249, vcc
	v_lshl_add_u32 v249, v249, 2, s18
	ds_read_b32 v249, v249
	v_readlane_b32 s10, v255, 40
	v_readlane_b32 s11, v255, 41
	v_readlane_b32 s22, v255, 42
	s_and_b64 s[10:11], s[8:9], s[10:11]
	v_readlane_b32 s23, v255, 43
	v_add_u32_e32 v250, v219, v184
	s_and_b64 vcc, s[10:11], s[22:23]
	v_cndmask_b32_e32 v250, v218, v250, vcc
	v_lshl_add_u32 v250, v250, 2, s18
	ds_read_b32 v250, v250
	v_readlane_b32 s10, v255, 44
	v_readlane_b32 s11, v255, 45
	s_and_b64 s[10:11], s[8:9], s[10:11]
	v_add_u32_e32 v251, v219, v185
	s_and_b64 vcc, s[10:11], s[30:31]
	v_cndmask_b32_e32 v251, v218, v251, vcc
	v_lshl_add_u32 v251, v251, 2, s18
	ds_read_b32 v251, v251
	s_and_b64 s[10:11], s[8:9], s[34:35]
	v_add_u32_e32 v252, v219, v186
	s_and_b64 vcc, s[10:11], s[24:25]
	v_cndmask_b32_e32 v252, v218, v252, vcc
	v_lshl_add_u32 v252, v252, 2, s18
	ds_read_b32 v252, v252
	s_and_b64 s[10:11], s[8:9], s[26:27]
	v_add_u32_e32 v253, v219, v187
	s_and_b64 vcc, s[10:11], s[28:29]
	v_cndmask_b32_e32 v253, v218, v253, vcc
	v_lshl_add_u32 v253, v253, 2, s18
	ds_read_b32 v253, v253
	s_and_b64 s[10:11], s[8:9], s[52:53]
	s_waitcnt lgkmcnt(14)
	v_add_f32_e32 v80, v80, v220
	v_add_u32_e32 v220, v219, v188
	s_and_b64 vcc, s[10:11], s[54:55]
	v_cndmask_b32_e32 v220, v218, v220, vcc
	v_lshl_add_u32 v220, v220, 2, s18
	ds_read_b32 v220, v220
	s_and_b64 s[10:11], s[8:9], s[56:57]
	s_waitcnt lgkmcnt(14)
	v_add_f32_e32 v81, v81, v221
	v_add_u32_e32 v221, v219, v189
	s_and_b64 vcc, s[10:11], s[58:59]
	v_cndmask_b32_e32 v221, v218, v221, vcc
	v_lshl_add_u32 v221, v221, 2, s18
	ds_read_b32 v221, v221
	s_and_b64 s[10:11], s[8:9], s[60:61]
	s_waitcnt lgkmcnt(14)
	v_add_f32_e32 v82, v82, v241
	v_add_u32_e32 v241, v219, v190
	s_and_b64 vcc, s[10:11], s[62:63]
	v_cndmask_b32_e32 v241, v218, v241, vcc
	v_lshl_add_u32 v241, v241, 2, s18
	ds_read_b32 v241, v241
	s_and_b64 s[10:11], s[8:9], s[64:65]
	s_waitcnt lgkmcnt(14)
	v_add_f32_e32 v83, v83, v242
	v_add_u32_e32 v242, v219, v191
	s_and_b64 vcc, s[10:11], s[66:67]
	v_cndmask_b32_e32 v242, v218, v242, vcc
	v_lshl_add_u32 v242, v242, 2, s18
	ds_read_b32 v242, v242
	s_and_b64 s[10:11], s[8:9], s[68:69]
	s_waitcnt lgkmcnt(14)
	v_add_f32_e32 v84, v84, v243
	v_add_u32_e32 v243, v219, v200
	s_and_b64 vcc, s[10:11], s[70:71]
	v_cndmask_b32_e32 v243, v218, v243, vcc
	v_lshl_add_u32 v243, v243, 2, s18
	ds_read_b32 v243, v243
	s_and_b64 s[10:11], s[8:9], s[72:73]
	s_waitcnt lgkmcnt(14)
	v_add_f32_e32 v85, v85, v244
	v_add_u32_e32 v244, v219, v201
	s_and_b64 vcc, s[10:11], s[74:75]
	v_cndmask_b32_e32 v244, v218, v244, vcc
	v_lshl_add_u32 v244, v244, 2, s18
	ds_read_b32 v244, v244
	s_and_b64 s[10:11], s[8:9], s[76:77]
	s_waitcnt lgkmcnt(14)
	v_add_f32_e32 v86, v86, v245
	v_add_u32_e32 v245, v219, v203
	s_and_b64 vcc, s[10:11], s[78:79]
	v_cndmask_b32_e32 v245, v218, v245, vcc
	v_lshl_add_u32 v245, v245, 2, s18
	ds_read_b32 v245, v245
	s_and_b64 s[10:11], s[8:9], s[80:81]
	s_waitcnt lgkmcnt(14)
	v_add_f32_e32 v87, v87, v246
	v_add_u32_e32 v246, v219, v204
	s_and_b64 vcc, s[10:11], s[82:83]
	v_cndmask_b32_e32 v246, v218, v246, vcc
	v_lshl_add_u32 v246, v246, 2, s18
	ds_read_b32 v246, v246
	s_and_b64 s[10:11], s[8:9], s[84:85]
	s_waitcnt lgkmcnt(14)
	v_add_f32_e32 v88, v88, v247
	v_add_u32_e32 v247, v219, v205
	s_and_b64 vcc, s[10:11], s[86:87]
	v_cndmask_b32_e32 v247, v218, v247, vcc
	v_lshl_add_u32 v247, v247, 2, s18
	ds_read_b32 v247, v247
	s_waitcnt lgkmcnt(14)
	v_add_f32_e32 v89, v89, v248
	v_add_u32_e32 v248, v219, v206
	s_and_b64 vcc, s[8:9], s[88:89]
	v_cndmask_b32_e32 v248, v218, v248, vcc
	v_lshl_add_u32 v248, v248, 2, s18
	ds_read_b32 v248, v248
	s_waitcnt lgkmcnt(14)
	v_add_f32_e32 v90, v90, v249
	v_add_u32_e32 v249, v219, v207
	s_and_b64 vcc, s[8:9], s[90:91]
	v_cndmask_b32_e32 v249, v218, v249, vcc
	v_lshl_add_u32 v249, v249, 2, s18
	ds_read_b32 v249, v249
	s_waitcnt lgkmcnt(14)
	v_add_f32_e32 v91, v91, v250
	v_add_u32_e32 v250, v219, v208
	s_and_b64 vcc, s[8:9], s[92:93]
	v_cndmask_b32_e32 v250, v218, v250, vcc
	v_lshl_add_u32 v250, v250, 2, s18
	ds_read_b32 v250, v250
	s_waitcnt lgkmcnt(14)
	v_add_f32_e32 v92, v92, v251
	v_add_u32_e32 v251, v219, v209
	s_and_b64 vcc, s[8:9], s[94:95]
	v_cndmask_b32_e32 v251, v218, v251, vcc
	v_lshl_add_u32 v251, v251, 2, s18
	ds_read_b32 v251, v251
	s_waitcnt lgkmcnt(14)
	v_add_f32_e32 v93, v93, v252
	v_add_u32_e32 v252, v219, v210
	s_and_b64 vcc, s[8:9], s[96:97]
	v_cndmask_b32_e32 v252, v218, v252, vcc
	v_lshl_add_u32 v252, v252, 2, s18
	ds_read_b32 v252, v252
	s_waitcnt lgkmcnt(14)
	v_add_f32_e32 v94, v94, v253
	v_add_u32_e32 v253, v219, v211
	s_and_b64 vcc, s[8:9], s[2:3]
	v_cndmask_b32_e32 v253, v218, v253, vcc
	v_lshl_add_u32 v253, v253, 2, s18
	ds_read_b32 v253, v253
	s_waitcnt lgkmcnt(14)
	v_add_f32_e32 v95, v95, v220
	v_add_u32_e32 v220, v219, v212
	s_and_b64 vcc, s[8:9], s[0:1]
	v_cndmask_b32_e32 v220, v218, v220, vcc
	v_lshl_add_u32 v220, v220, 2, s18
	ds_read_b32 v220, v220
	s_waitcnt lgkmcnt(14)
	v_add_f32_e32 v64, v64, v221
	v_add_u32_e32 v221, v219, v213
	s_and_b64 vcc, s[8:9], s[6:7]
	v_cndmask_b32_e32 v221, v218, v221, vcc
	v_lshl_add_u32 v221, v221, 2, s18
	ds_read_b32 v221, v221
	s_waitcnt lgkmcnt(14)
	v_add_f32_e32 v65, v65, v241
	s_waitcnt lgkmcnt(13)
	v_add_f32_e32 v66, v66, v242
	s_waitcnt lgkmcnt(12)
	v_add_f32_e32 v67, v67, v243
	s_waitcnt lgkmcnt(11)
	v_add_f32_e32 v68, v68, v244
	s_waitcnt lgkmcnt(10)
	v_add_f32_e32 v69, v69, v245
	s_waitcnt lgkmcnt(9)
	v_add_f32_e32 v70, v70, v246
	s_waitcnt lgkmcnt(8)
	v_add_f32_e32 v71, v71, v247
	s_waitcnt lgkmcnt(7)
	v_add_f32_e32 v72, v72, v248
	s_waitcnt lgkmcnt(6)
	v_add_f32_e32 v73, v73, v249
	s_waitcnt lgkmcnt(5)
	v_add_f32_e32 v74, v74, v250
	s_waitcnt lgkmcnt(4)
	v_add_f32_e32 v75, v75, v251
	s_waitcnt lgkmcnt(3)
	v_add_f32_e32 v76, v76, v252
	s_waitcnt lgkmcnt(2)
	v_add_f32_e32 v77, v77, v253
	s_waitcnt lgkmcnt(1)
	v_add_f32_e32 v78, v78, v220
	s_waitcnt lgkmcnt(0)
	v_add_f32_e32 v79, v79, v221

.Lna_deadA:
	v_add_f32_e32 v144, 0, v236
	v_add_f32_e32 v144, v238, v144
	v_add_f32_e32 v144, v145, v144
	v_add_f32_e32 v144, v237, v144
	v_add_f32_e32 v144, v146, v144
	v_add_f32_e32 v144, v235, v144
	v_add_f32_e32 v144, v147, v144
	v_add_f32_e32 v144, v234, v144
	v_add_f32_e32 v144, v231, v144
	v_add_f32_e32 v144, v233, v144
	v_add_f32_e32 v144, v230, v144
	v_add_f32_e32 v144, v232, v144
	v_exp_f32_e32 v134, v134
	v_add_f32_e32 v144, v227, v144
	v_exp_f32_e32 v135, v135
	v_add_f32_e32 v144, v229, v144
	v_exp_f32_e32 v138, v138
	v_add_f32_e32 v144, v226, v144
	v_exp_f32_e32 v139, v139
	v_add_f32_e32 v144, v228, v144
	v_exp_f32_e32 v130, v130
	v_add_f32_e32 v144, v134, v144
	v_exp_f32_e32 v131, v131
	v_add_f32_e32 v144, v135, v144
	v_exp_f32_e32 v132, v132
	v_add_f32_e32 v144, v138, v144
	v_exp_f32_e32 v133, v133
	v_add_f32_e32 v144, v139, v144
	v_exp_f32_e32 v136, v136
	v_add_f32_e32 v144, v130, v144
	v_exp_f32_e32 v137, v137
	v_add_f32_e32 v144, v131, v144
	v_exp_f32_e32 v142, v142
	v_add_f32_e32 v144, v132, v144
	v_exp_f32_e32 v143, v143
	v_add_f32_e32 v144, v133, v144
	v_exp_f32_e32 v140, v140
	v_add_f32_e32 v144, v136, v144
	v_exp_f32_e32 v141, v141
	v_add_f32_e32 v144, v137, v144
	v_exp_f32_e32 v128, v128
	v_add_f32_e32 v144, v142, v144
	v_exp_f32_e32 v129, v129
	v_add_f32_e32 v144, v143, v144
	v_add_f32_e32 v144, v140, v144
	v_add_f32_e32 v144, v141, v144
	v_add_f32_e32 v144, v128, v144
	v_add_f32_e32 v223, v129, v144
	v_mov_b32_e32 v224, v223
	v_cvt_pk_bf16_f32 v144, v236, v238
	v_cvt_pk_bf16_f32 v145, v145, v237
	v_cvt_pk_bf16_f32 v146, v146, v235
	s_nop 0
	v_permlane32_swap_b32_e32 v223, v224
	v_cvt_pk_bf16_f32 v147, v147, v234
	v_permlane32_swap_b32_e32 v144, v146
	v_cvt_pk_bf16_f32 v234, v231, v233
	v_cvt_pk_bf16_f32 v235, v230, v232
	v_cvt_pk_bf16_f32 v236, v227, v229
	v_cvt_pk_bf16_f32 v237, v226, v228
	v_cvt_pk_bf16_f32 v226, v134, v135
	v_cvt_pk_bf16_f32 v227, v138, v139
	v_cvt_pk_bf16_f32 v228, v130, v131
	v_cvt_pk_bf16_f32 v229, v132, v133
	v_cvt_pk_bf16_f32 v230, v136, v137
	v_cvt_pk_bf16_f32 v231, v142, v143
	v_cvt_pk_bf16_f32 v232, v140, v141
	v_cvt_pk_bf16_f32 v233, v128, v129
	v_permlane32_swap_b32_e32 v145, v147
	v_permlane32_swap_b32_e32 v234, v236
	v_permlane32_swap_b32_e32 v235, v237
	v_permlane32_swap_b32_e32 v226, v228
	v_permlane32_swap_b32_e32 v227, v229
	v_permlane32_swap_b32_e32 v230, v232
	v_permlane32_swap_b32_e32 v231, v233
	s_add_i32 s8, s19, 3
	s_cmp_lt_u32 s8, 12
	s_cselect_b64 s[10:11], -1, 0
	s_and_b64 s[8:9], s[10:11], exec
	s_cselect_b32 s8, 0, -12
	s_cselect_b32 s9, s13, 0x4000
	s_add_i32 s8, s8, s19
	s_lshl_b32 s8, s8, 6
	s_add_i32 s8, s8, s9
	s_mulk_i32 s8, 0x2400
	s_add_i32 s21, s8, 0x1b0000
	s_add_u32 s8, s14, s21
	s_addc_u32 s9, s15, 0
	s_add_u32 vcc_lo, s16, s21
	s_addc_u32 vcc_hi, s17, 0
	v_lshl_add_u64 v[128:129], vcc, 0, v[192:193]
	v_lshl_add_u64 v[132:133], vcc, 0, v[150:151]
	v_lshl_add_u64 v[136:137], s[8:9], 0, v[192:193]
	v_lshl_add_u64 v[140:141], s[8:9], 0, v[150:151]
	global_load_dwordx4 v[128:131], v[128:129], off
	s_nop 0
	global_load_dwordx4 v[132:135], v[132:133], off
	s_nop 0
	global_load_dwordx4 v[136:139], v[136:137], off
	s_nop 0
	global_load_dwordx4 v[140:143], v[140:141], off
	v_mov_b32_e32 v64, v217
	v_mov_b32_e32 v65, v217
	v_mov_b32_e32 v66, v217
	v_mov_b32_e32 v67, v217
	v_mov_b32_e32 v68, v217
	v_mov_b32_e32 v69, v217
	v_mov_b32_e32 v70, v217
	v_mov_b32_e32 v71, v217
	v_mov_b32_e32 v72, v217
	v_mov_b32_e32 v73, v217
	v_mov_b32_e32 v74, v217
	v_mov_b32_e32 v75, v217
	v_mov_b32_e32 v76, v217
	v_mov_b32_e32 v77, v217
	v_mov_b32_e32 v78, v217
	v_mov_b32_e32 v79, v217
	v_mov_b32_e32 v80, v217
	v_mov_b32_e32 v81, v217
	v_mov_b32_e32 v82, v217
	v_mov_b32_e32 v83, v217
	v_mov_b32_e32 v84, v217
	v_mov_b32_e32 v85, v217
	v_mov_b32_e32 v86, v217
	v_mov_b32_e32 v87, v217
	v_mov_b32_e32 v88, v217
	v_mov_b32_e32 v89, v217
	v_mov_b32_e32 v90, v217
	v_mov_b32_e32 v91, v217
	v_mov_b32_e32 v92, v217
	v_mov_b32_e32 v93, v217
	v_mov_b32_e32 v94, v217
	v_mov_b32_e32 v95, v217
	s_branch .LBB0_612
.Lna_deadB:
	s_andn2_b64 vcc, exec, s[10:11]
	v_exp_f32_e32 v249, v144
	v_add_f32_e32 v144, 0, v141
	v_add_f32_e32 v144, v143, v144
	v_add_f32_e32 v144, v139, v144
	v_add_f32_e32 v144, v142, v144
	v_add_f32_e32 v144, v137, v144
	v_add_f32_e32 v144, v140, v144
	v_add_f32_e32 v144, v136, v144
	v_add_f32_e32 v144, v138, v144
	v_add_f32_e32 v144, v133, v144
	v_add_f32_e32 v144, v135, v144
	v_add_f32_e32 v144, v131, v144
	v_add_f32_e32 v144, v134, v144
	v_exp_f32_e32 v218, v145
	v_add_f32_e32 v144, v129, v144
	v_exp_f32_e32 v219, v146
	v_add_f32_e32 v144, v132, v144
	v_exp_f32_e32 v220, v147
	v_add_f32_e32 v144, v128, v144
	v_exp_f32_e32 v221, v226
	v_add_f32_e32 v144, v130, v144
	v_exp_f32_e32 v238, v227
	v_add_f32_e32 v144, v218, v144
	v_exp_f32_e32 v241, v228
	v_add_f32_e32 v144, v219, v144
	v_exp_f32_e32 v242, v229
	v_add_f32_e32 v144, v220, v144
	v_exp_f32_e32 v243, v230
	v_add_f32_e32 v144, v221, v144
	v_exp_f32_e32 v244, v231
	v_add_f32_e32 v144, v238, v144
	v_exp_f32_e32 v245, v232
	v_add_f32_e32 v144, v241, v144
	v_exp_f32_e32 v246, v233
	v_add_f32_e32 v144, v242, v144
	v_exp_f32_e32 v247, v234
	v_add_f32_e32 v144, v243, v144
	v_exp_f32_e32 v248, v235
	v_add_f32_e32 v144, v244, v144
	v_exp_f32_e32 v236, v236
	v_add_f32_e32 v144, v245, v144
	v_exp_f32_e32 v237, v237
	v_add_f32_e32 v144, v246, v144
	v_add_f32_e32 v144, v247, v144
	v_add_f32_e32 v144, v248, v144
	v_add_f32_e32 v144, v236, v144
	v_add_f32_e32 v144, v237, v144
	v_add_f32_e32 v239, v249, v144
	v_mov_b32_e32 v240, v239
	v_cvt_pk_bf16_f32 v144, v141, v143
	v_cvt_pk_bf16_f32 v145, v139, v142
	v_cvt_pk_bf16_f32 v146, v137, v140
	v_cvt_pk_bf16_f32 v147, v136, v138
	s_nop 1
	v_permlane32_swap_b32_e32 v239, v240
	v_permlane32_swap_b32_e32 v144, v146
	v_permlane32_swap_b32_e32 v145, v147
	v_cvt_pk_bf16_f32 v226, v133, v135
	v_cvt_pk_bf16_f32 v227, v131, v134
	v_cvt_pk_bf16_f32 v228, v129, v132
	v_cvt_pk_bf16_f32 v229, v128, v130
	v_cvt_pk_bf16_f32 v230, v218, v219
	v_cvt_pk_bf16_f32 v231, v220, v221
	v_cvt_pk_bf16_f32 v232, v238, v241
	v_cvt_pk_bf16_f32 v233, v242, v243
	v_cvt_pk_bf16_f32 v234, v244, v245
	v_cvt_pk_bf16_f32 v235, v246, v247
	v_cvt_pk_bf16_f32 v236, v248, v236
	v_cvt_pk_bf16_f32 v237, v237, v249
	s_nop 0
	v_permlane32_swap_b32_e32 v226, v228
	v_permlane32_swap_b32_e32 v227, v229
	v_permlane32_swap_b32_e32 v230, v232
	v_permlane32_swap_b32_e32 v231, v233
	v_permlane32_swap_b32_e32 v234, v236
	v_permlane32_swap_b32_e32 v235, v237
	s_cmp_lt_u32 s20, 10
	s_cselect_b32 s8, 0, -12
	s_cselect_b32 s9, s13, 0x4000
	s_add_i32 s8, s8, s19
	s_lshl_b32 s8, s8, 6
	s_add_i32 s8, s8, s9
	s_mulk_i32 s8, 0x2400
	s_add_i32 s10, s8, 0x240000
	s_add_u32 s8, s14, s10
	s_addc_u32 s9, s15, 0
	s_add_u32 s10, s16, s10
	s_addc_u32 s11, s17, 0
	v_lshl_add_u64 v[128:129], s[10:11], 0, v[192:193]
	v_lshl_add_u64 v[132:133], s[10:11], 0, v[150:151]
	v_lshl_add_u64 v[136:137], s[8:9], 0, v[192:193]
	v_lshl_add_u64 v[140:141], s[8:9], 0, v[150:151]
	global_load_dwordx4 v[128:131], v[128:129], off
	s_nop 0
	global_load_dwordx4 v[132:135], v[132:133], off
	s_nop 0
	global_load_dwordx4 v[136:139], v[136:137], off
	s_nop 0
	global_load_dwordx4 v[140:143], v[140:141], off
	v_mov_b32_e32 v64, v217
	v_mov_b32_e32 v65, v217
	v_mov_b32_e32 v66, v217
	v_mov_b32_e32 v67, v217
	v_mov_b32_e32 v68, v217
	v_mov_b32_e32 v69, v217
	v_mov_b32_e32 v70, v217
	v_mov_b32_e32 v71, v217
	v_mov_b32_e32 v72, v217
	v_mov_b32_e32 v73, v217
	v_mov_b32_e32 v74, v217
	v_mov_b32_e32 v75, v217
	v_mov_b32_e32 v76, v217
	v_mov_b32_e32 v77, v217
	v_mov_b32_e32 v78, v217
	v_mov_b32_e32 v79, v217
	v_mov_b32_e32 v80, v217
	v_mov_b32_e32 v81, v217
	v_mov_b32_e32 v82, v217
	v_mov_b32_e32 v83, v217
	v_mov_b32_e32 v84, v217
	v_mov_b32_e32 v85, v217
	v_mov_b32_e32 v86, v217
	v_mov_b32_e32 v87, v217
	v_mov_b32_e32 v88, v217
	v_mov_b32_e32 v89, v217
	v_mov_b32_e32 v90, v217
	v_mov_b32_e32 v91, v217
	v_mov_b32_e32 v92, v217
	v_mov_b32_e32 v93, v217
	v_mov_b32_e32 v94, v217
	v_mov_b32_e32 v95, v217
	s_branch .LBB0_618
